# baseline (speedup 1.0000x reference)
_Z11edge_kernelILi36ELb1EEvPKfS1_PKDF16_PKiS5_S1_S1_S1_S1_S1_PDF16_:
	s_load_dwordx8 s[4:11], s[0:1], 0x0
	s_load_dwordx8 s[12:19], s[0:1], 0x20
	s_load_dwordx4 s[20:23], s[0:1], 0x40
	s_load_dwordx2 s[24:25], s[0:1], 0x50
	v_readfirstlane_b32 s3, v0
	v_bfe_u32 v139, v0, 4, 2
	v_and_b32_e32 v140, 15, v0
	v_and_b32_e32 v142, 63, v0
	s_lshr_b32 s3, s3, 6
	s_lshl_b32 s2, s2, 1
	s_add_i32 s2, s2, s3
	v_lshlrev_b32_e32 v138, 8, v139
	v_lshl_or_b32 v138, v140, 4, v138
	v_lshlrev_b32_e32 v143, 4, v142
	v_lshl_or_b32 v141, v140, 2, v139
	v_lshlrev_b32_e32 v141, 2, v141
	v_mul_u32_u24_e32 v137, 0x900, v139
	v_lshl_or_b32 v137, v140, 4, v137
	v_mul_u32_u24_e32 v142, 36, v139
	s_mul_i32 s28, s2, 0x2400
	s_lshl_b32 s29, s2, 14
	s_lshl_b32 s30, s2, 2
	s_lshl_b32 s31, s2, 8
	s_lshl_b32 s33, s3, 10
	s_lshl_b32 s34, s3, 8
	s_addk_i32 s34, 0x4000
	s_waitcnt lgkmcnt(0)
	s_add_u32 s10, s10, s30
	s_addc_u32 s11, s11, 0
	s_add_u32 s12, s12, s30
	s_addc_u32 s13, s13, 0
	s_load_dword s35, s[10:11], 0x0
	s_load_dword s36, s[12:13], 0x0
	s_add_u32 s14, s14, s28
	s_addc_u32 s15, s15, 0
	global_load_dwordx4 v[0:3], v137, s[14:15] nt
	global_load_dwordx4 v[4:7], v137, s[14:15] offset:256 nt
	global_load_dwordx4 v[8:11], v137, s[14:15] offset:512 nt
	global_load_dwordx4 v[12:15], v137, s[14:15] offset:768 nt
	global_load_dwordx4 v[16:19], v137, s[14:15] offset:1024 nt
	global_load_dwordx4 v[20:23], v137, s[14:15] offset:1280 nt
	global_load_dwordx4 v[24:27], v137, s[14:15] offset:1536 nt
	global_load_dwordx4 v[28:31], v137, s[14:15] offset:1792 nt
	global_load_dwordx4 v[32:35], v137, s[14:15] offset:2048 nt
	s_add_u32 s22, s22, s33
	s_addc_u32 s23, s23, 0
	s_mov_b32 m0, s33
	s_add_u32 s18, s18, s29
	s_addc_u32 s19, s19, 0
	global_load_lds_dwordx4 v143, s[22:23]
	global_load_lds_dwordx4 v143, s[22:23]
	global_load_lds_dwordx4 v143, s[22:23] offset:2048
	global_load_lds_dwordx4 v143, s[22:23] offset:2048
	s_add_u32 m0, m0, 0x1000
	s_add_u32 s22, s22, 0x1000
	s_addc_u32 s23, s23, 0
	global_load_lds_dwordx4 v143, s[22:23]
	global_load_lds_dwordx4 v143, s[22:23]
	global_load_lds_dwordx4 v143, s[22:23] offset:2048
	global_load_lds_dwordx4 v143, s[22:23] offset:2048
	s_add_u32 m0, m0, 0x1000
	s_add_u32 s22, s22, 0x1000
	s_addc_u32 s23, s23, 0
	global_load_lds_dwordx4 v143, s[22:23]
	global_load_lds_dwordx4 v143, s[22:23]
	global_load_lds_dwordx4 v143, s[22:23] offset:2048
	global_load_lds_dwordx4 v143, s[22:23] offset:2048
	s_add_u32 m0, m0, 0x1000
	s_add_u32 s22, s22, 0x1000
	s_addc_u32 s23, s23, 0
	global_load_lds_dwordx4 v143, s[22:23]
	global_load_lds_dwordx4 v143, s[22:23]
	global_load_lds_dwordx4 v143, s[22:23] offset:2048
	global_load_lds_dwordx4 v143, s[22:23] offset:2048
	s_add_u32 s16, s16, s31
	s_addc_u32 s17, s17, 0
	s_add_u32 s20, s20, s31
	s_addc_u32 s21, s21, 0
	s_waitcnt lgkmcnt(0)
	s_lshl_b32 s36, s36, 7
	s_add_u32 s24, s24, s36
	s_addc_u32 s25, s25, 0
	s_lshl_b32 s37, s35, 7
	s_lshl_b32 s38, s35, 4
	s_add_u32 s4, s4, s37
	s_addc_u32 s5, s5, 0
	s_add_u32 s6, s6, s38
	s_addc_u32 s7, s7, 0
	v_mov_b32_e32 v157, 0
	v_mov_b32_e32 v156, v142
	v_lshl_add_u64 v[158:159], s[4:5], 0, v[156:157]
	v_lshl_add_u64 v[158:159], v[158:159], 0, 20
	v_cmp_eq_u32_e32 vcc, 3, v139
	s_nop 1
	v_mov_b32_e32 v154, s6
	v_mov_b32_e32 v155, s7
	v_cndmask_b32_e32 v158, v158, v154, vcc
	v_cndmask_b32_e32 v159, v159, v155, vcc
	global_load_dwordx4 v[144:147], v142, s[4:5] nt
	global_load_dword v148, v142, s[4:5] offset:16 nt
	global_load_dwordx4 v[150:153], v[158:159], off nt
	global_load_dword v136, v141, s[16:17] nt
	global_load_dword v128, v141, s[20:21] nt
	global_load_dwordx4 v[64:67], v138, s[18:19] nt
	global_load_dwordx4 v[68:71], v138, s[18:19] offset:1024 nt
	global_load_dwordx4 v[72:75], v138, s[18:19] offset:2048 nt
	global_load_dwordx4 v[76:79], v138, s[18:19] offset:3072 nt
	s_add_u32 s18, s18, 0x1000
	s_addc_u32 s19, s19, 0
	global_load_dwordx4 v[80:83], v138, s[18:19] nt
	global_load_dwordx4 v[84:87], v138, s[18:19] offset:1024 nt
	global_load_dwordx4 v[88:91], v138, s[18:19] offset:2048 nt
	global_load_dwordx4 v[92:95], v138, s[18:19] offset:3072 nt
	s_add_u32 s18, s18, 0x1000
	s_addc_u32 s19, s19, 0
	global_load_dwordx4 v[96:99], v138, s[18:19] nt
	global_load_dwordx4 v[100:103], v138, s[18:19] offset:1024 nt
	global_load_dwordx4 v[104:107], v138, s[18:19] offset:2048 nt
	global_load_dwordx4 v[108:111], v138, s[18:19] offset:3072 nt
	s_add_u32 s18, s18, 0x1000
	s_addc_u32 s19, s19, 0
	global_load_dwordx4 v[112:115], v138, s[18:19] nt
	global_load_dwordx4 v[116:119], v138, s[18:19] offset:1024 nt
	global_load_dwordx4 v[120:123], v138, s[18:19] offset:2048 nt
	global_load_dwordx4 v[124:127], v138, s[18:19] offset:3072 nt
	v_add_u32_e32 v142, s34, v141
	v_lshl_add_u32 v143, v139, 2, s34
	s_waitcnt vmcnt(18)
	s_barrier
	v_pk_mul_f32 v[160:161], v[144:145], v[0:1] op_sel_hi:[0,1]
	v_pk_mul_f32 v[162:163], v[144:145], v[2:3] op_sel_hi:[0,1]
	v_pk_mul_f32 v[164:165], v[144:145], v[4:5] op_sel:[1,0]
	v_pk_mul_f32 v[166:167], v[144:145], v[6:7] op_sel:[1,0]
	v_pk_fma_f32 v[160:161], v[146:147], v[8:9], v[160:161] op_sel_hi:[0,1,1]
	v_pk_fma_f32 v[162:163], v[146:147], v[10:11], v[162:163] op_sel_hi:[0,1,1]
	v_pk_fma_f32 v[164:165], v[146:147], v[12:13], v[164:165] op_sel:[1,0,0]
	v_pk_fma_f32 v[166:167], v[146:147], v[14:15], v[166:167] op_sel:[1,0,0]
	v_pk_fma_f32 v[160:161], v[148:149], v[16:17], v[160:161] op_sel_hi:[0,1,1]
	v_pk_fma_f32 v[162:163], v[148:149], v[18:19], v[162:163] op_sel_hi:[0,1,1]
	v_pk_fma_f32 v[164:165], v[150:151], v[20:21], v[164:165] op_sel_hi:[0,1,1]
	v_pk_fma_f32 v[166:167], v[150:151], v[22:23], v[166:167] op_sel_hi:[0,1,1]
	v_pk_fma_f32 v[160:161], v[150:151], v[24:25], v[160:161] op_sel:[1,0,0]
	v_pk_fma_f32 v[162:163], v[150:151], v[26:27], v[162:163] op_sel:[1,0,0]
	v_pk_fma_f32 v[164:165], v[152:153], v[28:29], v[164:165] op_sel_hi:[0,1,1]
	v_pk_fma_f32 v[166:167], v[152:153], v[30:31], v[166:167] op_sel_hi:[0,1,1]
	v_pk_fma_f32 v[160:161], v[152:153], v[32:33], v[160:161] op_sel:[1,0,0]
	v_pk_fma_f32 v[162:163], v[152:153], v[34:35], v[162:163] op_sel:[1,0,0]
	v_pk_add_f32 v[160:161], v[160:161], v[164:165]
	v_pk_add_f32 v[162:163], v[162:163], v[166:167]
	s_nop 1
	v_permlane16_swap_b32_e32 v160, v161
	v_permlane16_swap_b32_e32 v162, v163
	v_add_f32_e32 v160, v160, v161
	v_add_f32_e32 v162, v162, v163
	s_nop 1
	v_permlane32_swap_b32_e32 v160, v162
	v_add_f32_e32 v160, v160, v162
	s_waitcnt vmcnt(17)
	v_add_f32_e32 v160, v160, v136
	v_max_f32_e32 v160, 0, v160
	ds_write_b32 v142, v160
	ds_read2_b32 v[144:145], v143 offset0:0 offset1:4
	ds_read2_b32 v[146:147], v143 offset0:8 offset1:12
	ds_read2_b32 v[148:149], v143 offset0:16 offset1:20
	ds_read2_b32 v[150:151], v143 offset0:24 offset1:28
	ds_read2_b32 v[152:153], v143 offset0:32 offset1:36
	ds_read2_b32 v[154:155], v143 offset0:40 offset1:44
	ds_read2_b32 v[156:157], v143 offset0:48 offset1:52
	ds_read2_b32 v[158:159], v143 offset0:56 offset1:60
	ds_read_b128 v[0:3], v138
	ds_read_b128 v[4:7], v138 offset:1024
	ds_read_b128 v[8:11], v138 offset:2048
	ds_read_b128 v[12:15], v138 offset:3072
	ds_read_b128 v[16:19], v138 offset:4096
	ds_read_b128 v[20:23], v138 offset:5120
	s_waitcnt lgkmcnt(6)
	s_waitcnt vmcnt(12)
	v_pk_mul_f32 v[160:161], v[144:145], v[64:65] op_sel_hi:[0,1]
	v_pk_mul_f32 v[162:163], v[144:145], v[66:67] op_sel_hi:[0,1]
	v_pk_mul_f32 v[164:165], v[144:145], v[68:69] op_sel:[1,0]
	v_pk_mul_f32 v[166:167], v[144:145], v[70:71] op_sel:[1,0]
	v_pk_fma_f32 v[160:161], v[146:147], v[72:73], v[160:161] op_sel_hi:[0,1,1]
	v_pk_fma_f32 v[162:163], v[146:147], v[74:75], v[162:163] op_sel_hi:[0,1,1]
	v_pk_fma_f32 v[164:165], v[146:147], v[76:77], v[164:165] op_sel:[1,0,0]
	v_pk_fma_f32 v[166:167], v[146:147], v[78:79], v[166:167] op_sel:[1,0,0]
	ds_read_b128 v[24:27], v138 offset:6144
	ds_read_b128 v[28:31], v138 offset:7168
	ds_read_b128 v[32:35], v138 offset:8192
	ds_read_b128 v[36:39], v138 offset:9216
	ds_read_b128 v[40:43], v138 offset:10240
	ds_read_b128 v[44:47], v138 offset:11264
	s_waitcnt vmcnt(8)
	v_pk_fma_f32 v[160:161], v[148:149], v[80:81], v[160:161] op_sel_hi:[0,1,1]
	v_pk_fma_f32 v[162:163], v[148:149], v[82:83], v[162:163] op_sel_hi:[0,1,1]
	v_pk_fma_f32 v[164:165], v[148:149], v[84:85], v[164:165] op_sel:[1,0,0]
	v_pk_fma_f32 v[166:167], v[148:149], v[86:87], v[166:167] op_sel:[1,0,0]
	v_pk_fma_f32 v[160:161], v[150:151], v[88:89], v[160:161] op_sel_hi:[0,1,1]
	v_pk_fma_f32 v[162:163], v[150:151], v[90:91], v[162:163] op_sel_hi:[0,1,1]
	v_pk_fma_f32 v[164:165], v[150:151], v[92:93], v[164:165] op_sel:[1,0,0]
	v_pk_fma_f32 v[166:167], v[150:151], v[94:95], v[166:167] op_sel:[1,0,0]
	s_waitcnt lgkmcnt(4)
	ds_read_b128 v[48:51], v138 offset:12288
	ds_read_b128 v[52:55], v138 offset:13312
	ds_read_b128 v[56:59], v138 offset:14336
	ds_read_b128 v[60:63], v138 offset:15360
	s_waitcnt vmcnt(4)
	v_pk_fma_f32 v[160:161], v[152:153], v[96:97], v[160:161] op_sel_hi:[0,1,1]
	v_pk_fma_f32 v[162:163], v[152:153], v[98:99], v[162:163] op_sel_hi:[0,1,1]
	v_pk_fma_f32 v[164:165], v[152:153], v[100:101], v[164:165] op_sel:[1,0,0]
	v_pk_fma_f32 v[166:167], v[152:153], v[102:103], v[166:167] op_sel:[1,0,0]
	v_pk_fma_f32 v[160:161], v[154:155], v[104:105], v[160:161] op_sel_hi:[0,1,1]
	v_pk_fma_f32 v[162:163], v[154:155], v[106:107], v[162:163] op_sel_hi:[0,1,1]
	v_pk_fma_f32 v[164:165], v[154:155], v[108:109], v[164:165] op_sel:[1,0,0]
	v_pk_fma_f32 v[166:167], v[154:155], v[110:111], v[166:167] op_sel:[1,0,0]
	s_waitcnt vmcnt(0)
	v_pk_fma_f32 v[160:161], v[156:157], v[112:113], v[160:161] op_sel_hi:[0,1,1]
	v_pk_fma_f32 v[162:163], v[156:157], v[114:115], v[162:163] op_sel_hi:[0,1,1]
	v_pk_fma_f32 v[164:165], v[156:157], v[116:117], v[164:165] op_sel:[1,0,0]
	v_pk_fma_f32 v[166:167], v[156:157], v[118:119], v[166:167] op_sel:[1,0,0]
	v_pk_fma_f32 v[160:161], v[158:159], v[120:121], v[160:161] op_sel_hi:[0,1,1]
	v_pk_fma_f32 v[162:163], v[158:159], v[122:123], v[162:163] op_sel_hi:[0,1,1]
	v_pk_fma_f32 v[164:165], v[158:159], v[124:125], v[164:165] op_sel:[1,0,0]
	v_pk_fma_f32 v[166:167], v[158:159], v[126:127], v[166:167] op_sel:[1,0,0]
	v_pk_add_f32 v[160:161], v[160:161], v[164:165]
	v_pk_add_f32 v[162:163], v[162:163], v[166:167]
	s_nop 1
	v_permlane16_swap_b32_e32 v160, v161
	v_permlane16_swap_b32_e32 v162, v163
	v_add_f32_e32 v160, v160, v161
	v_add_f32_e32 v162, v162, v163
	s_nop 1
	v_permlane32_swap_b32_e32 v160, v162
	v_add_f32_e32 v160, v160, v162
	v_add_f32_e32 v160, v160, v128
	s_waitcnt lgkmcnt(0)
	ds_write_b32 v142, v160
	ds_read2_b32 v[144:145], v143 offset0:0 offset1:4
	ds_read2_b32 v[146:147], v143 offset0:8 offset1:12
	ds_read2_b32 v[148:149], v143 offset0:16 offset1:20
	ds_read2_b32 v[150:151], v143 offset0:24 offset1:28
	ds_read2_b32 v[152:153], v143 offset0:32 offset1:36
	ds_read2_b32 v[154:155], v143 offset0:40 offset1:44
	ds_read2_b32 v[156:157], v143 offset0:48 offset1:52
	ds_read2_b32 v[158:159], v143 offset0:56 offset1:60
	v_lshlrev_b32_e32 v136, 3, v140
	v_lshl_or_b32 v136, v139, 2, v136
	v_cmp_gt_u32_e32 vcc, 2, v139
	s_waitcnt lgkmcnt(0)
	v_pk_mul_f32 v[160:161], v[144:145], v[0:1] op_sel_hi:[0,1]
	v_pk_mul_f32 v[162:163], v[144:145], v[2:3] op_sel_hi:[0,1]
	v_pk_mul_f32 v[164:165], v[144:145], v[4:5] op_sel:[1,0]
	v_pk_mul_f32 v[166:167], v[144:145], v[6:7] op_sel:[1,0]
	v_pk_fma_f32 v[160:161], v[146:147], v[8:9], v[160:161] op_sel_hi:[0,1,1]
	v_pk_fma_f32 v[162:163], v[146:147], v[10:11], v[162:163] op_sel_hi:[0,1,1]
	v_pk_fma_f32 v[164:165], v[146:147], v[12:13], v[164:165] op_sel:[1,0,0]
	v_pk_fma_f32 v[166:167], v[146:147], v[14:15], v[166:167] op_sel:[1,0,0]
	v_pk_fma_f32 v[160:161], v[148:149], v[16:17], v[160:161] op_sel_hi:[0,1,1]
	v_pk_fma_f32 v[162:163], v[148:149], v[18:19], v[162:163] op_sel_hi:[0,1,1]
	v_pk_fma_f32 v[164:165], v[148:149], v[20:21], v[164:165] op_sel:[1,0,0]
	v_pk_fma_f32 v[166:167], v[148:149], v[22:23], v[166:167] op_sel:[1,0,0]
	v_pk_fma_f32 v[160:161], v[150:151], v[24:25], v[160:161] op_sel_hi:[0,1,1]
	v_pk_fma_f32 v[162:163], v[150:151], v[26:27], v[162:163] op_sel_hi:[0,1,1]
	v_pk_fma_f32 v[164:165], v[150:151], v[28:29], v[164:165] op_sel:[1,0,0]
	v_pk_fma_f32 v[166:167], v[150:151], v[30:31], v[166:167] op_sel:[1,0,0]
	v_pk_fma_f32 v[160:161], v[152:153], v[32:33], v[160:161] op_sel_hi:[0,1,1]
	v_pk_fma_f32 v[162:163], v[152:153], v[34:35], v[162:163] op_sel_hi:[0,1,1]
	v_pk_fma_f32 v[164:165], v[152:153], v[36:37], v[164:165] op_sel:[1,0,0]
	v_pk_fma_f32 v[166:167], v[152:153], v[38:39], v[166:167] op_sel:[1,0,0]
	v_pk_fma_f32 v[160:161], v[154:155], v[40:41], v[160:161] op_sel_hi:[0,1,1]
	v_pk_fma_f32 v[162:163], v[154:155], v[42:43], v[162:163] op_sel_hi:[0,1,1]
	v_pk_fma_f32 v[164:165], v[154:155], v[44:45], v[164:165] op_sel:[1,0,0]
	v_pk_fma_f32 v[166:167], v[154:155], v[46:47], v[166:167] op_sel:[1,0,0]
	v_pk_fma_f32 v[160:161], v[156:157], v[48:49], v[160:161] op_sel_hi:[0,1,1]
	v_pk_fma_f32 v[162:163], v[156:157], v[50:51], v[162:163] op_sel_hi:[0,1,1]
	v_pk_fma_f32 v[164:165], v[156:157], v[52:53], v[164:165] op_sel:[1,0,0]
	v_pk_fma_f32 v[166:167], v[156:157], v[54:55], v[166:167] op_sel:[1,0,0]
	v_pk_fma_f32 v[160:161], v[158:159], v[56:57], v[160:161] op_sel_hi:[0,1,1]
	v_pk_fma_f32 v[162:163], v[158:159], v[58:59], v[162:163] op_sel_hi:[0,1,1]
	v_pk_fma_f32 v[164:165], v[158:159], v[60:61], v[164:165] op_sel:[1,0,0]
	v_pk_fma_f32 v[166:167], v[158:159], v[62:63], v[166:167] op_sel:[1,0,0]
	v_pk_add_f32 v[160:161], v[160:161], v[164:165]
	v_pk_add_f32 v[162:163], v[162:163], v[166:167]
	s_nop 1
	v_permlane16_swap_b32_e32 v160, v162
	v_permlane16_swap_b32_e32 v161, v163
	v_add_f32_e32 v160, v160, v162
	v_add_f32_e32 v161, v161, v163
	v_mov_b32_e32 v144, v160
	v_mov_b32_e32 v145, v161
	s_nop 1
	v_permlane32_swap_b32_e32 v160, v144
	v_permlane32_swap_b32_e32 v161, v145
	v_add_f32_e32 v160, v160, v144
	v_add_f32_e32 v161, v161, v145
	v_cvt_pk_f16_f32 v137, v160, v161
	s_and_saveexec_b64 s[4:5], vcc
	global_atomic_pk_add_f16 v136, v137, s[24:25]
	s_endpgm
	.p2align	8

_Z11edge_kernelILi64ELb0EEvPKfS1_PKDF16_PKiS5_S1_S1_S1_S1_S1_PDF16_:
	s_load_dwordx16 s[4:19], s[0:1], 0x10
	s_load_dwordx2 s[20:21], s[0:1], 0x50
	v_readfirstlane_b32 s3, v0
	v_bfe_u32 v139, v0, 4, 2
	v_and_b32_e32 v140, 15, v0
	v_and_b32_e32 v142, 63, v0
	s_lshr_b32 s3, s3, 6
	s_lshl_b32 s2, s2, 1
	s_add_i32 s2, s2, s3
	v_lshlrev_b32_e32 v138, 8, v139
	v_lshl_or_b32 v138, v140, 4, v138
	v_lshlrev_b32_e32 v143, 4, v142
	v_lshl_or_b32 v141, v140, 2, v139
	v_lshlrev_b32_e32 v141, 2, v141
	v_lshlrev_b32_e32 v142, 5, v139
	v_lshlrev_b32_e32 v137, 12, v139
	v_lshl_or_b32 v137, v140, 4, v137
	s_lshl_b32 s28, s2, 14
	s_lshl_b32 s29, s2, 14
	s_lshl_b32 s30, s2, 2
	s_lshl_b32 s31, s2, 8
	s_lshl_b32 s33, s3, 10
	s_lshl_b32 s34, s3, 8
	s_addk_i32 s34, 0x4000
	s_waitcnt lgkmcnt(0)
	s_add_u32 s6, s6, s30
	s_addc_u32 s7, s7, 0
	s_add_u32 s8, s8, s30
	s_addc_u32 s9, s9, 0
	s_load_dword s35, s[6:7], 0x0
	s_load_dword s36, s[8:9], 0x0
	s_add_u32 s10, s10, s28
	s_addc_u32 s11, s11, 0
	global_load_dwordx4 v[0:3], v137, s[10:11] nt
	global_load_dwordx4 v[4:7], v137, s[10:11] offset:256 nt
	global_load_dwordx4 v[8:11], v137, s[10:11] offset:512 nt
	global_load_dwordx4 v[12:15], v137, s[10:11] offset:768 nt
	global_load_dwordx4 v[16:19], v137, s[10:11] offset:1024 nt
	global_load_dwordx4 v[20:23], v137, s[10:11] offset:1280 nt
	global_load_dwordx4 v[24:27], v137, s[10:11] offset:1536 nt
	global_load_dwordx4 v[28:31], v137, s[10:11] offset:1792 nt
	global_load_dwordx4 v[32:35], v137, s[10:11] offset:2048 nt
	global_load_dwordx4 v[36:39], v137, s[10:11] offset:2304 nt
	global_load_dwordx4 v[40:43], v137, s[10:11] offset:2560 nt
	global_load_dwordx4 v[44:47], v137, s[10:11] offset:2816 nt
	global_load_dwordx4 v[48:51], v137, s[10:11] offset:3072 nt
	global_load_dwordx4 v[52:55], v137, s[10:11] offset:3328 nt
	global_load_dwordx4 v[56:59], v137, s[10:11] offset:3584 nt
	global_load_dwordx4 v[60:63], v137, s[10:11] offset:3840 nt
	s_add_u32 s18, s18, s33
	s_addc_u32 s19, s19, 0
	s_mov_b32 m0, s33
	s_add_u32 s14, s14, s29
	s_addc_u32 s15, s15, 0
	global_load_lds_dwordx4 v143, s[18:19]
	global_load_lds_dwordx4 v143, s[18:19]
	global_load_lds_dwordx4 v143, s[18:19] offset:2048
	global_load_lds_dwordx4 v143, s[18:19] offset:2048
	s_add_u32 m0, m0, 0x1000
	s_add_u32 s18, s18, 0x1000
	s_addc_u32 s19, s19, 0
	global_load_lds_dwordx4 v143, s[18:19]
	global_load_lds_dwordx4 v143, s[18:19]
	global_load_lds_dwordx4 v143, s[18:19] offset:2048
	global_load_lds_dwordx4 v143, s[18:19] offset:2048
	s_add_u32 m0, m0, 0x1000
	s_add_u32 s18, s18, 0x1000
	s_addc_u32 s19, s19, 0
	global_load_lds_dwordx4 v143, s[18:19]
	global_load_lds_dwordx4 v143, s[18:19]
	global_load_lds_dwordx4 v143, s[18:19] offset:2048
	global_load_lds_dwordx4 v143, s[18:19] offset:2048
	s_add_u32 m0, m0, 0x1000
	s_add_u32 s18, s18, 0x1000
	s_addc_u32 s19, s19, 0
	global_load_lds_dwordx4 v143, s[18:19]
	global_load_lds_dwordx4 v143, s[18:19]
	global_load_lds_dwordx4 v143, s[18:19] offset:2048
	global_load_lds_dwordx4 v143, s[18:19] offset:2048
	s_add_u32 s12, s12, s31
	s_addc_u32 s13, s13, 0
	s_add_u32 s16, s16, s31
	s_addc_u32 s17, s17, 0
	s_waitcnt lgkmcnt(0)
	s_lshl_b32 s36, s36, 7
	s_add_u32 s20, s20, s36
	s_addc_u32 s21, s21, 0
	s_lshl_b32 s37, s35, 7
	s_add_u32 s4, s4, s37
	s_addc_u32 s5, s5, 0
	global_load_dwordx4 v[128:131], v142, s[4:5] nt
	global_load_dwordx4 v[132:135], v142, s[4:5] offset:16 nt
	global_load_dword v136, v141, s[12:13] nt
	global_load_dword v137, v141, s[16:17] nt
	global_load_dwordx4 v[64:67], v138, s[14:15] nt
	global_load_dwordx4 v[68:71], v138, s[14:15] offset:1024 nt
	global_load_dwordx4 v[72:75], v138, s[14:15] offset:2048 nt
	global_load_dwordx4 v[76:79], v138, s[14:15] offset:3072 nt
	s_add_u32 s14, s14, 0x1000
	s_addc_u32 s15, s15, 0
	global_load_dwordx4 v[80:83], v138, s[14:15] nt
	global_load_dwordx4 v[84:87], v138, s[14:15] offset:1024 nt
	global_load_dwordx4 v[88:91], v138, s[14:15] offset:2048 nt
	global_load_dwordx4 v[92:95], v138, s[14:15] offset:3072 nt
	s_add_u32 s14, s14, 0x1000
	s_addc_u32 s15, s15, 0
	global_load_dwordx4 v[96:99], v138, s[14:15] nt
	global_load_dwordx4 v[100:103], v138, s[14:15] offset:1024 nt
	global_load_dwordx4 v[104:107], v138, s[14:15] offset:2048 nt
	global_load_dwordx4 v[108:111], v138, s[14:15] offset:3072 nt
	s_add_u32 s14, s14, 0x1000
	s_addc_u32 s15, s15, 0
	global_load_dwordx4 v[112:115], v138, s[14:15] nt
	global_load_dwordx4 v[116:119], v138, s[14:15] offset:1024 nt
	global_load_dwordx4 v[120:123], v138, s[14:15] offset:2048 nt
	global_load_dwordx4 v[124:127], v138, s[14:15] offset:3072 nt
	v_add_u32_e32 v142, s34, v141
	v_lshl_add_u32 v143, v139, 2, s34
	s_waitcnt vmcnt(18)
	s_barrier
	v_cvt_f32_f16_e32 v144, v128
	v_cvt_f32_f16_sdwa v145, v128 dst_sel:DWORD dst_unused:UNUSED_PAD src0_sel:WORD_1
	v_cvt_f32_f16_e32 v146, v129
	v_cvt_f32_f16_sdwa v147, v129 dst_sel:DWORD dst_unused:UNUSED_PAD src0_sel:WORD_1
	v_cvt_f32_f16_e32 v148, v130
	v_cvt_f32_f16_sdwa v149, v130 dst_sel:DWORD dst_unused:UNUSED_PAD src0_sel:WORD_1
	v_cvt_f32_f16_e32 v150, v131
	v_cvt_f32_f16_sdwa v151, v131 dst_sel:DWORD dst_unused:UNUSED_PAD src0_sel:WORD_1
	v_cvt_f32_f16_e32 v152, v132
	v_cvt_f32_f16_sdwa v153, v132 dst_sel:DWORD dst_unused:UNUSED_PAD src0_sel:WORD_1
	v_cvt_f32_f16_e32 v154, v133
	v_cvt_f32_f16_sdwa v155, v133 dst_sel:DWORD dst_unused:UNUSED_PAD src0_sel:WORD_1
	v_cvt_f32_f16_e32 v156, v134
	v_cvt_f32_f16_sdwa v157, v134 dst_sel:DWORD dst_unused:UNUSED_PAD src0_sel:WORD_1
	v_cvt_f32_f16_e32 v158, v135
	v_cvt_f32_f16_sdwa v159, v135 dst_sel:DWORD dst_unused:UNUSED_PAD src0_sel:WORD_1
	v_max_f32_e32 v144, 0, v144
	v_max_f32_e32 v145, 0, v145
	v_max_f32_e32 v146, 0, v146
	v_max_f32_e32 v147, 0, v147
	v_max_f32_e32 v148, 0, v148
	v_max_f32_e32 v149, 0, v149
	v_max_f32_e32 v150, 0, v150
	v_max_f32_e32 v151, 0, v151
	v_max_f32_e32 v152, 0, v152
	v_max_f32_e32 v153, 0, v153
	v_max_f32_e32 v154, 0, v154
	v_max_f32_e32 v155, 0, v155
	v_max_f32_e32 v156, 0, v156
	v_max_f32_e32 v157, 0, v157
	v_max_f32_e32 v158, 0, v158
	v_max_f32_e32 v159, 0, v159
	v_pk_mul_f32 v[160:161], v[144:145], v[0:1] op_sel_hi:[0,1]
	v_pk_mul_f32 v[162:163], v[144:145], v[2:3] op_sel_hi:[0,1]
	v_pk_mul_f32 v[164:165], v[144:145], v[4:5] op_sel:[1,0]
	v_pk_mul_f32 v[166:167], v[144:145], v[6:7] op_sel:[1,0]
	v_pk_fma_f32 v[160:161], v[146:147], v[8:9], v[160:161] op_sel_hi:[0,1,1]
	v_pk_fma_f32 v[162:163], v[146:147], v[10:11], v[162:163] op_sel_hi:[0,1,1]
	v_pk_fma_f32 v[164:165], v[146:147], v[12:13], v[164:165] op_sel:[1,0,0]
	v_pk_fma_f32 v[166:167], v[146:147], v[14:15], v[166:167] op_sel:[1,0,0]
	v_pk_fma_f32 v[160:161], v[148:149], v[16:17], v[160:161] op_sel_hi:[0,1,1]
	v_pk_fma_f32 v[162:163], v[148:149], v[18:19], v[162:163] op_sel_hi:[0,1,1]
	v_pk_fma_f32 v[164:165], v[148:149], v[20:21], v[164:165] op_sel:[1,0,0]
	v_pk_fma_f32 v[166:167], v[148:149], v[22:23], v[166:167] op_sel:[1,0,0]
	v_pk_fma_f32 v[160:161], v[150:151], v[24:25], v[160:161] op_sel_hi:[0,1,1]
	v_pk_fma_f32 v[162:163], v[150:151], v[26:27], v[162:163] op_sel_hi:[0,1,1]
	v_pk_fma_f32 v[164:165], v[150:151], v[28:29], v[164:165] op_sel:[1,0,0]
	v_pk_fma_f32 v[166:167], v[150:151], v[30:31], v[166:167] op_sel:[1,0,0]
	v_pk_fma_f32 v[160:161], v[152:153], v[32:33], v[160:161] op_sel_hi:[0,1,1]
	v_pk_fma_f32 v[162:163], v[152:153], v[34:35], v[162:163] op_sel_hi:[0,1,1]
	v_pk_fma_f32 v[164:165], v[152:153], v[36:37], v[164:165] op_sel:[1,0,0]
	v_pk_fma_f32 v[166:167], v[152:153], v[38:39], v[166:167] op_sel:[1,0,0]
	v_pk_fma_f32 v[160:161], v[154:155], v[40:41], v[160:161] op_sel_hi:[0,1,1]
	v_pk_fma_f32 v[162:163], v[154:155], v[42:43], v[162:163] op_sel_hi:[0,1,1]
	v_pk_fma_f32 v[164:165], v[154:155], v[44:45], v[164:165] op_sel:[1,0,0]
	v_pk_fma_f32 v[166:167], v[154:155], v[46:47], v[166:167] op_sel:[1,0,0]
	v_pk_fma_f32 v[160:161], v[156:157], v[48:49], v[160:161] op_sel_hi:[0,1,1]
	v_pk_fma_f32 v[162:163], v[156:157], v[50:51], v[162:163] op_sel_hi:[0,1,1]
	v_pk_fma_f32 v[164:165], v[156:157], v[52:53], v[164:165] op_sel:[1,0,0]
	v_pk_fma_f32 v[166:167], v[156:157], v[54:55], v[166:167] op_sel:[1,0,0]
	v_pk_fma_f32 v[160:161], v[158:159], v[56:57], v[160:161] op_sel_hi:[0,1,1]
	v_pk_fma_f32 v[162:163], v[158:159], v[58:59], v[162:163] op_sel_hi:[0,1,1]
	v_pk_fma_f32 v[164:165], v[158:159], v[60:61], v[164:165] op_sel:[1,0,0]
	v_pk_fma_f32 v[166:167], v[158:159], v[62:63], v[166:167] op_sel:[1,0,0]
	v_pk_add_f32 v[160:161], v[160:161], v[164:165]
	v_pk_add_f32 v[162:163], v[162:163], v[166:167]
	s_nop 1
	v_permlane16_swap_b32_e32 v160, v161
	v_permlane16_swap_b32_e32 v162, v163
	v_add_f32_e32 v160, v160, v161
	v_add_f32_e32 v162, v162, v163
	s_nop 1
	v_permlane32_swap_b32_e32 v160, v162
	v_add_f32_e32 v160, v160, v162
	s_waitcnt vmcnt(17)
	v_add_f32_e32 v160, v160, v136
	v_max_f32_e32 v160, 0, v160
	ds_write_b32 v142, v160
	ds_read2_b32 v[144:145], v143 offset0:0 offset1:4
	ds_read2_b32 v[146:147], v143 offset0:8 offset1:12
	ds_read2_b32 v[148:149], v143 offset0:16 offset1:20
	ds_read2_b32 v[150:151], v143 offset0:24 offset1:28
	ds_read2_b32 v[152:153], v143 offset0:32 offset1:36
	ds_read2_b32 v[154:155], v143 offset0:40 offset1:44
	ds_read2_b32 v[156:157], v143 offset0:48 offset1:52
	ds_read2_b32 v[158:159], v143 offset0:56 offset1:60
	ds_read_b128 v[0:3], v138
	ds_read_b128 v[4:7], v138 offset:1024
	ds_read_b128 v[8:11], v138 offset:2048
	ds_read_b128 v[12:15], v138 offset:3072
	ds_read_b128 v[16:19], v138 offset:4096
	ds_read_b128 v[20:23], v138 offset:5120
	s_waitcnt lgkmcnt(6)
	s_waitcnt vmcnt(12)
	v_pk_mul_f32 v[160:161], v[144:145], v[64:65] op_sel_hi:[0,1]
	v_pk_mul_f32 v[162:163], v[144:145], v[66:67] op_sel_hi:[0,1]
	v_pk_mul_f32 v[164:165], v[144:145], v[68:69] op_sel:[1,0]
	v_pk_mul_f32 v[166:167], v[144:145], v[70:71] op_sel:[1,0]
	v_pk_fma_f32 v[160:161], v[146:147], v[72:73], v[160:161] op_sel_hi:[0,1,1]
	v_pk_fma_f32 v[162:163], v[146:147], v[74:75], v[162:163] op_sel_hi:[0,1,1]
	v_pk_fma_f32 v[164:165], v[146:147], v[76:77], v[164:165] op_sel:[1,0,0]
	v_pk_fma_f32 v[166:167], v[146:147], v[78:79], v[166:167] op_sel:[1,0,0]
	ds_read_b128 v[24:27], v138 offset:6144
	ds_read_b128 v[28:31], v138 offset:7168
	ds_read_b128 v[32:35], v138 offset:8192
	ds_read_b128 v[36:39], v138 offset:9216
	ds_read_b128 v[40:43], v138 offset:10240
	ds_read_b128 v[44:47], v138 offset:11264
	s_waitcnt vmcnt(8)
	v_pk_fma_f32 v[160:161], v[148:149], v[80:81], v[160:161] op_sel_hi:[0,1,1]
	v_pk_fma_f32 v[162:163], v[148:149], v[82:83], v[162:163] op_sel_hi:[0,1,1]
	v_pk_fma_f32 v[164:165], v[148:149], v[84:85], v[164:165] op_sel:[1,0,0]
	v_pk_fma_f32 v[166:167], v[148:149], v[86:87], v[166:167] op_sel:[1,0,0]
	v_pk_fma_f32 v[160:161], v[150:151], v[88:89], v[160:161] op_sel_hi:[0,1,1]
	v_pk_fma_f32 v[162:163], v[150:151], v[90:91], v[162:163] op_sel_hi:[0,1,1]
	v_pk_fma_f32 v[164:165], v[150:151], v[92:93], v[164:165] op_sel:[1,0,0]
	v_pk_fma_f32 v[166:167], v[150:151], v[94:95], v[166:167] op_sel:[1,0,0]
	s_waitcnt lgkmcnt(4)
	ds_read_b128 v[48:51], v138 offset:12288
	ds_read_b128 v[52:55], v138 offset:13312
	ds_read_b128 v[56:59], v138 offset:14336
	ds_read_b128 v[60:63], v138 offset:15360
	s_waitcnt vmcnt(4)
	v_pk_fma_f32 v[160:161], v[152:153], v[96:97], v[160:161] op_sel_hi:[0,1,1]
	v_pk_fma_f32 v[162:163], v[152:153], v[98:99], v[162:163] op_sel_hi:[0,1,1]
	v_pk_fma_f32 v[164:165], v[152:153], v[100:101], v[164:165] op_sel:[1,0,0]
	v_pk_fma_f32 v[166:167], v[152:153], v[102:103], v[166:167] op_sel:[1,0,0]
	v_pk_fma_f32 v[160:161], v[154:155], v[104:105], v[160:161] op_sel_hi:[0,1,1]
	v_pk_fma_f32 v[162:163], v[154:155], v[106:107], v[162:163] op_sel_hi:[0,1,1]
	v_pk_fma_f32 v[164:165], v[154:155], v[108:109], v[164:165] op_sel:[1,0,0]
	v_pk_fma_f32 v[166:167], v[154:155], v[110:111], v[166:167] op_sel:[1,0,0]
	s_waitcnt vmcnt(0)
	v_pk_fma_f32 v[160:161], v[156:157], v[112:113], v[160:161] op_sel_hi:[0,1,1]
	v_pk_fma_f32 v[162:163], v[156:157], v[114:115], v[162:163] op_sel_hi:[0,1,1]
	v_pk_fma_f32 v[164:165], v[156:157], v[116:117], v[164:165] op_sel:[1,0,0]
	v_pk_fma_f32 v[166:167], v[156:157], v[118:119], v[166:167] op_sel:[1,0,0]
	v_pk_fma_f32 v[160:161], v[158:159], v[120:121], v[160:161] op_sel_hi:[0,1,1]
	v_pk_fma_f32 v[162:163], v[158:159], v[122:123], v[162:163] op_sel_hi:[0,1,1]
	v_pk_fma_f32 v[164:165], v[158:159], v[124:125], v[164:165] op_sel:[1,0,0]
	v_pk_fma_f32 v[166:167], v[158:159], v[126:127], v[166:167] op_sel:[1,0,0]
	v_pk_add_f32 v[160:161], v[160:161], v[164:165]
	v_pk_add_f32 v[162:163], v[162:163], v[166:167]
	s_nop 1
	v_permlane16_swap_b32_e32 v160, v161
	v_permlane16_swap_b32_e32 v162, v163
	v_add_f32_e32 v160, v160, v161
	v_add_f32_e32 v162, v162, v163
	s_nop 1
	v_permlane32_swap_b32_e32 v160, v162
	v_add_f32_e32 v160, v160, v162
	v_add_f32_e32 v160, v160, v137
	s_waitcnt lgkmcnt(0)
	ds_write_b32 v142, v160
	ds_read2_b32 v[144:145], v143 offset0:0 offset1:4
	ds_read2_b32 v[146:147], v143 offset0:8 offset1:12
	ds_read2_b32 v[148:149], v143 offset0:16 offset1:20
	ds_read2_b32 v[150:151], v143 offset0:24 offset1:28
	ds_read2_b32 v[152:153], v143 offset0:32 offset1:36
	ds_read2_b32 v[154:155], v143 offset0:40 offset1:44
	ds_read2_b32 v[156:157], v143 offset0:48 offset1:52
	ds_read2_b32 v[158:159], v143 offset0:56 offset1:60
	v_lshlrev_b32_e32 v136, 3, v140
	v_lshl_or_b32 v136, v139, 2, v136
	v_cmp_gt_u32_e32 vcc, 2, v139
	s_waitcnt lgkmcnt(0)
	v_pk_mul_f32 v[160:161], v[144:145], v[0:1] op_sel_hi:[0,1]
	v_pk_mul_f32 v[162:163], v[144:145], v[2:3] op_sel_hi:[0,1]
	v_pk_mul_f32 v[164:165], v[144:145], v[4:5] op_sel:[1,0]
	v_pk_mul_f32 v[166:167], v[144:145], v[6:7] op_sel:[1,0]
	v_pk_fma_f32 v[160:161], v[146:147], v[8:9], v[160:161] op_sel_hi:[0,1,1]
	v_pk_fma_f32 v[162:163], v[146:147], v[10:11], v[162:163] op_sel_hi:[0,1,1]
	v_pk_fma_f32 v[164:165], v[146:147], v[12:13], v[164:165] op_sel:[1,0,0]
	v_pk_fma_f32 v[166:167], v[146:147], v[14:15], v[166:167] op_sel:[1,0,0]
	v_pk_fma_f32 v[160:161], v[148:149], v[16:17], v[160:161] op_sel_hi:[0,1,1]
	v_pk_fma_f32 v[162:163], v[148:149], v[18:19], v[162:163] op_sel_hi:[0,1,1]
	v_pk_fma_f32 v[164:165], v[148:149], v[20:21], v[164:165] op_sel:[1,0,0]
	v_pk_fma_f32 v[166:167], v[148:149], v[22:23], v[166:167] op_sel:[1,0,0]
	v_pk_fma_f32 v[160:161], v[150:151], v[24:25], v[160:161] op_sel_hi:[0,1,1]
	v_pk_fma_f32 v[162:163], v[150:151], v[26:27], v[162:163] op_sel_hi:[0,1,1]
	v_pk_fma_f32 v[164:165], v[150:151], v[28:29], v[164:165] op_sel:[1,0,0]
	v_pk_fma_f32 v[166:167], v[150:151], v[30:31], v[166:167] op_sel:[1,0,0]
	v_pk_fma_f32 v[160:161], v[152:153], v[32:33], v[160:161] op_sel_hi:[0,1,1]
	v_pk_fma_f32 v[162:163], v[152:153], v[34:35], v[162:163] op_sel_hi:[0,1,1]
	v_pk_fma_f32 v[164:165], v[152:153], v[36:37], v[164:165] op_sel:[1,0,0]
	v_pk_fma_f32 v[166:167], v[152:153], v[38:39], v[166:167] op_sel:[1,0,0]
	v_pk_fma_f32 v[160:161], v[154:155], v[40:41], v[160:161] op_sel_hi:[0,1,1]
	v_pk_fma_f32 v[162:163], v[154:155], v[42:43], v[162:163] op_sel_hi:[0,1,1]
	v_pk_fma_f32 v[164:165], v[154:155], v[44:45], v[164:165] op_sel:[1,0,0]
	v_pk_fma_f32 v[166:167], v[154:155], v[46:47], v[166:167] op_sel:[1,0,0]
	v_pk_fma_f32 v[160:161], v[156:157], v[48:49], v[160:161] op_sel_hi:[0,1,1]
	v_pk_fma_f32 v[162:163], v[156:157], v[50:51], v[162:163] op_sel_hi:[0,1,1]
	v_pk_fma_f32 v[164:165], v[156:157], v[52:53], v[164:165] op_sel:[1,0,0]
	v_pk_fma_f32 v[166:167], v[156:157], v[54:55], v[166:167] op_sel:[1,0,0]
	v_pk_fma_f32 v[160:161], v[158:159], v[56:57], v[160:161] op_sel_hi:[0,1,1]
	v_pk_fma_f32 v[162:163], v[158:159], v[58:59], v[162:163] op_sel_hi:[0,1,1]
	v_pk_fma_f32 v[164:165], v[158:159], v[60:61], v[164:165] op_sel:[1,0,0]
	v_pk_fma_f32 v[166:167], v[158:159], v[62:63], v[166:167] op_sel:[1,0,0]
	v_pk_add_f32 v[160:161], v[160:161], v[164:165]
	v_pk_add_f32 v[162:163], v[162:163], v[166:167]
	s_nop 1
	v_permlane16_swap_b32_e32 v160, v162
	v_permlane16_swap_b32_e32 v161, v163
	v_add_f32_e32 v160, v160, v162
	v_add_f32_e32 v161, v161, v163
	v_mov_b32_e32 v144, v160
	v_mov_b32_e32 v145, v161
	s_nop 1
	v_permlane32_swap_b32_e32 v160, v144
	v_permlane32_swap_b32_e32 v161, v145
	v_add_f32_e32 v160, v160, v144
	v_add_f32_e32 v161, v161, v145
	v_cvt_pk_f16_f32 v137, v160, v161
	s_and_saveexec_b64 s[4:5], vcc
	global_atomic_pk_add_f16 v136, v137, s[20:21]
	s_endpgm
	.p2align	8
